# DSA steady loop: redundant phase-A lgkmcnt waits (K fragments already retired by the previous step's barrier wait) removed, mask-word addresses by one 64-bit add; on top of table mask + trims
# speedup vs baseline: 1.0134x; 1.0134x over previous
.LBB0_1077:
	v_lshl_add_u64 v[14:15], v[184:185], 0, s[54:55]
	s_mov_b64 s[38:39], 0xeb20000
	v_lshl_add_u64 v[2:3], v[14:15], 0, s[38:39]
	s_mov_b64 s[38:39], 0xeb28000
	v_add_u32_e32 v12, s29, v239
	v_lshl_add_u64 v[4:5], v[14:15], 0, s[38:39]
	global_load_dword v0, v[2:3], off
	global_load_dword v190, v[4:5], off
	global_load_dword v191, v[182:183], off offset:-4
	v_lshrrev_b32_e32 v2, v238, v211
	v_lshrrev_b32_e32 v3, v238, v213
	v_bfe_u32 v4, v2, 0, 4
	v_lshl_add_u32 v4, v4, 4, s100
	ds_read_b128 v[80:83], v4
	v_bfe_u32 v4, v2, 8, 4
	v_lshl_add_u32 v4, v4, 4, s100
	ds_read_b128 v[84:87], v4
	v_bfe_u32 v4, v2, 16, 4
	v_lshl_add_u32 v4, v4, 4, s100
	ds_read_b128 v[88:91], v4
	v_bfe_u32 v4, v2, 24, 4
	v_lshl_add_u32 v4, v4, 4, s100
	ds_read_b128 v[92:95], v4
	v_bfe_u32 v4, v3, 0, 4
	v_lshl_add_u32 v4, v4, 4, s100
	ds_read_b128 v[96:99], v4
	v_bfe_u32 v4, v3, 8, 4
	v_lshl_add_u32 v4, v4, 4, s100
	ds_read_b128 v[100:103], v4
	v_bfe_u32 v4, v3, 16, 4
	v_lshl_add_u32 v4, v4, 4, s100
	ds_read_b128 v[104:107], v4
	v_bfe_u32 v4, v3, 24, 4
	v_lshl_add_u32 v4, v4, 4, s100
	ds_read_b128 v[108:111], v4
	ds_read_b64_tr_b16 v[176:177], v12 offset:24576
	ds_read_b64_tr_b16 v[178:179], v12 offset:25088
	s_waitcnt lgkmcnt(6)
	v_mfma_f32_32x32x16_bf16 v[80:95], v[172:175], v[124:127], v[80:95]
	v_add_f32_e32 v2, v64, v65
	v_add_f32_e32 v2, v66, v2
	v_add_f32_e32 v2, v67, v2
	v_add_f32_e32 v2, v68, v2
	v_add_f32_e32 v2, v69, v2
	v_cvt_pk_bf16_f32 v140, v64, v65
	v_cvt_pk_bf16_f32 v141, v66, v67
	ds_read_b64_tr_b16 v[172:173], v12 offset:28672
	ds_read_b64_tr_b16 v[174:175], v12 offset:29184
	s_waitcnt lgkmcnt(4)
	v_mfma_f32_32x32x16_bf16 v[96:111], v[164:167], v[124:127], v[96:111]
	v_add_f32_e32 v2, v70, v2
	v_add_f32_e32 v2, v71, v2
	v_add_f32_e32 v2, v72, v2
	v_add_f32_e32 v2, v73, v2
	v_cvt_pk_bf16_f32 v142, v68, v69
	v_cvt_pk_bf16_f32 v143, v70, v71
	ds_read_b64_tr_b16 v[164:165], v12 offset:25600
	ds_read_b64_tr_b16 v[166:167], v12 offset:26112
	v_mfma_f32_32x32x16_bf16 v[80:95], v[168:171], v[120:123], v[80:95]
	v_add_f32_e32 v2, v74, v2
	v_add_f32_e32 v2, v75, v2
	v_add_f32_e32 v2, v76, v2
	v_add_f32_e32 v2, v77, v2
	v_cvt_pk_bf16_f32 v136, v72, v73
	v_cvt_pk_bf16_f32 v137, v74, v75
	ds_read_b64_tr_b16 v[168:169], v12 offset:29696
	ds_read_b64_tr_b16 v[170:171], v12 offset:30208
	v_mfma_f32_32x32x16_bf16 v[96:111], v[160:163], v[120:123], v[96:111]
	v_add_f32_e32 v2, v78, v2
	v_add_f32_e32 v2, v79, v2
	v_add_f32_e32 v2, v48, v2
	v_add_f32_e32 v2, v49, v2
	v_cvt_pk_bf16_f32 v138, v76, v77
	v_cvt_pk_bf16_f32 v139, v78, v79
	ds_read_b64_tr_b16 v[160:161], v12 offset:26624
	ds_read_b64_tr_b16 v[162:163], v12 offset:27136
	v_mfma_f32_32x32x16_bf16 v[80:95], v[156:159], v[116:119], v[80:95]
	v_add_f32_e32 v2, v50, v2
	v_add_f32_e32 v2, v51, v2
	v_add_f32_e32 v2, v52, v2
	v_add_f32_e32 v6, v53, v2
	v_cvt_pk_bf16_f32 v132, v48, v49
	v_cvt_pk_bf16_f32 v133, v50, v51
	ds_read_b64_tr_b16 v[2:3], v12 offset:30720
	ds_read_b64_tr_b16 v[4:5], v12 offset:31232
	v_mfma_f32_32x32x16_bf16 v[96:111], v[152:155], v[116:119], v[96:111]
	v_add_f32_e32 v6, v54, v6
	v_add_f32_e32 v6, v55, v6
	v_add_f32_e32 v6, v56, v6
	v_add_f32_e32 v10, v57, v6
	v_cvt_pk_bf16_f32 v134, v52, v53
	v_cvt_pk_bf16_f32 v135, v54, v55
	ds_read_b64_tr_b16 v[6:7], v12 offset:27648
	ds_read_b64_tr_b16 v[8:9], v12 offset:28160
	v_mfma_f32_32x32x16_bf16 v[80:95], v[148:151], v[112:115], v[80:95]
	v_add_f32_e32 v10, v58, v10
	v_add_f32_e32 v10, v59, v10
	v_add_f32_e32 v10, v60, v10
	v_add_f32_e32 v48, v61, v10
	v_cvt_pk_bf16_f32 v128, v56, v57
	v_cvt_pk_bf16_f32 v129, v58, v59
	ds_read_b64_tr_b16 v[10:11], v12 offset:31744
	ds_read_b64_tr_b16 v[12:13], v12 offset:32256
	v_mfma_f32_32x32x16_bf16 v[96:111], v[144:147], v[112:115], v[96:111]
	v_add_f32_e32 v48, v62, v48
	v_add_f32_e32 v48, v63, v48
	v_cvt_pk_bf16_f32 v130, v60, v61
	v_cvt_pk_bf16_f32 v131, v62, v63
	v_lshl_add_u64 v[186:187], v[216:217], 0, s[54:55]
	v_lshl_add_u64 v[50:51], v[186:187], 0, s[20:21]
	s_add_i32 s29, s59, s63
	s_mov_b32 m0, s29
	s_nop 0
	global_load_lds_dwordx4 v[50:51], off
	v_lshl_add_u64 v[188:189], v[218:219], 0, s[54:55]
	v_lshl_add_u64 v[50:51], v[188:189], 0, s[24:25]
	s_add_i32 s29, s57, s62
	s_mov_b32 m0, s29
	s_nop 0
	global_load_lds_dwordx4 v[50:51], off
	s_waitcnt vmcnt(7)
	v_mul_f32_e32 v49, v201, v209
	v_cmp_nge_f32_e32 vcc, s73, v49
	v_cmp_neq_f32_e64 s[38:39], 0, v207
	s_or_b64 vcc, vcc, s[38:39]
	s_cmp_lg_u64 vcc, 0
	s_cselect_b64 s[38:39], -1, 0
	s_cbranch_vccz .LBB0_1079
	v_sub_f32_e32 v95, v95, v207
	v_sub_f32_e32 v94, v94, v207
	v_sub_f32_e32 v93, v93, v207
	v_sub_f32_e32 v92, v92, v207
	v_sub_f32_e32 v91, v91, v207
	v_sub_f32_e32 v90, v90, v207
	v_sub_f32_e32 v89, v89, v207
	v_sub_f32_e32 v88, v88, v207
	v_sub_f32_e32 v87, v87, v207
	v_sub_f32_e32 v86, v86, v207
	v_sub_f32_e32 v85, v85, v207
	v_sub_f32_e32 v84, v84, v207
	v_sub_f32_e32 v83, v83, v207
	v_sub_f32_e32 v82, v82, v207
	v_sub_f32_e32 v81, v81, v207
	v_sub_f32_e32 v80, v80, v207
	v_sub_f32_e32 v111, v111, v207
	v_sub_f32_e32 v110, v110, v207
	v_sub_f32_e32 v109, v109, v207
	v_sub_f32_e32 v108, v108, v207
	v_sub_f32_e32 v107, v107, v207
	v_sub_f32_e32 v106, v106, v207
	v_sub_f32_e32 v105, v105, v207
	v_sub_f32_e32 v104, v104, v207
	v_sub_f32_e32 v103, v103, v207
	v_sub_f32_e32 v102, v102, v207
	v_sub_f32_e32 v101, v101, v207
	v_sub_f32_e32 v100, v100, v207
	v_sub_f32_e32 v99, v99, v207
	v_sub_f32_e32 v98, v98, v207
	v_sub_f32_e32 v97, v97, v207
	v_sub_f32_e32 v96, v96, v207

.LBB0_1082:
	s_add_i32 s29, s57, 0x2000
	s_cmpk_lg_i32 s57, 0x4000
	s_cselect_b32 s65, s29, 0
	s_mov_b64 s[38:39], 0xeb30000
	v_add_u32_e32 v12, s59, v239
	v_lshl_add_u64 v[2:3], v[14:15], 0, s[38:39]
	global_load_dword v192, v[2:3], off
	s_mov_b64 s[38:39], 0xeb38000
	v_lshl_add_u64 v[2:3], v[14:15], 0, s[38:39]
	global_load_dword v14, v[2:3], off
	global_load_dword v209, v[182:183], off
	v_lshrrev_b32_e32 v2, v238, v0
	v_lshrrev_b32_e32 v3, v238, v190
	v_bfe_u32 v4, v2, 0, 4
	v_lshl_add_u32 v4, v4, 4, s100
	ds_read_b128 v[80:83], v4
	v_bfe_u32 v4, v2, 8, 4
	v_lshl_add_u32 v4, v4, 4, s100
	ds_read_b128 v[84:87], v4
	v_bfe_u32 v4, v2, 16, 4
	v_lshl_add_u32 v4, v4, 4, s100
	ds_read_b128 v[88:91], v4
	v_bfe_u32 v4, v2, 24, 4
	v_lshl_add_u32 v4, v4, 4, s100
	ds_read_b128 v[92:95], v4
	v_bfe_u32 v4, v3, 0, 4
	v_lshl_add_u32 v4, v4, 4, s100
	ds_read_b128 v[96:99], v4
	v_bfe_u32 v4, v3, 8, 4
	v_lshl_add_u32 v4, v4, 4, s100
	ds_read_b128 v[100:103], v4
	v_bfe_u32 v4, v3, 16, 4
	v_lshl_add_u32 v4, v4, 4, s100
	ds_read_b128 v[104:107], v4
	v_bfe_u32 v4, v3, 24, 4
	v_lshl_add_u32 v4, v4, 4, s100
	ds_read_b128 v[108:111], v4
	ds_read_b64_tr_b16 v[156:157], v12 offset:24576
	ds_read_b64_tr_b16 v[158:159], v12 offset:25088
	s_waitcnt lgkmcnt(6)
	v_mfma_f32_32x32x16_bf16 v[80:95], v[140:143], v[124:127], v[80:95]
	v_add_f32_e32 v2, v64, v65
	v_add_f32_e32 v2, v66, v2
	v_add_f32_e32 v2, v67, v2
	v_add_f32_e32 v2, v68, v2
	v_add_f32_e32 v2, v69, v2
	v_cvt_pk_bf16_f32 v140, v64, v65
	v_cvt_pk_bf16_f32 v141, v66, v67
	ds_read_b64_tr_b16 v[152:153], v12 offset:28672
	ds_read_b64_tr_b16 v[154:155], v12 offset:29184
	s_waitcnt lgkmcnt(4)
	v_mfma_f32_32x32x16_bf16 v[96:111], v[136:139], v[124:127], v[96:111]
	v_add_f32_e32 v2, v70, v2
	v_add_f32_e32 v2, v71, v2
	v_add_f32_e32 v2, v72, v2
	v_add_f32_e32 v2, v73, v2
	v_cvt_pk_bf16_f32 v142, v68, v69
	v_cvt_pk_bf16_f32 v143, v70, v71
	ds_read_b64_tr_b16 v[144:145], v12 offset:25600
	ds_read_b64_tr_b16 v[146:147], v12 offset:26112
	v_mfma_f32_32x32x16_bf16 v[80:95], v[148:151], v[120:123], v[80:95]
	v_add_f32_e32 v2, v74, v2
	v_add_f32_e32 v2, v75, v2
	v_add_f32_e32 v2, v76, v2
	v_add_f32_e32 v2, v77, v2
	v_cvt_pk_bf16_f32 v136, v72, v73
	v_cvt_pk_bf16_f32 v137, v74, v75
	ds_read_b64_tr_b16 v[148:149], v12 offset:29696
	ds_read_b64_tr_b16 v[150:151], v12 offset:30208
	v_mfma_f32_32x32x16_bf16 v[96:111], v[176:179], v[120:123], v[96:111]
	v_add_f32_e32 v2, v78, v2
	v_add_f32_e32 v2, v79, v2
	v_add_f32_e32 v2, v48, v2
	v_add_f32_e32 v2, v49, v2
	v_cvt_pk_bf16_f32 v138, v76, v77
	v_cvt_pk_bf16_f32 v139, v78, v79
	ds_read_b64_tr_b16 v[176:177], v12 offset:26624
	ds_read_b64_tr_b16 v[178:179], v12 offset:27136
	v_mfma_f32_32x32x16_bf16 v[80:95], v[172:175], v[116:119], v[80:95]
	v_add_f32_e32 v2, v50, v2
	v_add_f32_e32 v2, v51, v2
	v_add_f32_e32 v2, v52, v2
	v_add_f32_e32 v6, v53, v2
	v_cvt_pk_bf16_f32 v132, v48, v49
	v_cvt_pk_bf16_f32 v133, v50, v51
	ds_read_b64_tr_b16 v[2:3], v12 offset:30720
	ds_read_b64_tr_b16 v[4:5], v12 offset:31232
	v_mfma_f32_32x32x16_bf16 v[96:111], v[164:167], v[116:119], v[96:111]
	v_add_f32_e32 v6, v54, v6
	v_add_f32_e32 v6, v55, v6
	v_add_f32_e32 v6, v56, v6
	v_add_f32_e32 v10, v57, v6
	v_cvt_pk_bf16_f32 v134, v52, v53
	v_cvt_pk_bf16_f32 v135, v54, v55
	ds_read_b64_tr_b16 v[6:7], v12 offset:27648
	ds_read_b64_tr_b16 v[8:9], v12 offset:28160
	v_mfma_f32_32x32x16_bf16 v[80:95], v[168:171], v[112:115], v[80:95]
	v_add_f32_e32 v10, v58, v10
	v_add_f32_e32 v10, v59, v10
	v_add_f32_e32 v10, v60, v10
	v_add_f32_e32 v15, v61, v10
	v_cvt_pk_bf16_f32 v128, v56, v57
	v_cvt_pk_bf16_f32 v129, v58, v59
	ds_read_b64_tr_b16 v[10:11], v12 offset:31744
	ds_read_b64_tr_b16 v[12:13], v12 offset:32256
	v_mfma_f32_32x32x16_bf16 v[96:111], v[160:163], v[112:115], v[96:111]
	v_add_f32_e32 v15, v62, v15
	v_add_f32_e32 v15, v63, v15
	v_cvt_pk_bf16_f32 v130, v60, v61
	v_cvt_pk_bf16_f32 v131, v62, v63
	v_lshl_add_u64 v[48:49], v[186:187], 0, s[22:23]
	s_add_i32 s29, s57, s63
	s_mov_b32 m0, s29
	s_nop 0
	global_load_lds_dwordx4 v[48:49], off
	v_lshl_add_u64 v[48:49], v[188:189], 0, s[70:71]
	s_add_i32 s29, s65, s62
	s_mov_b32 m0, s29
	s_nop 0
	global_load_lds_dwordx4 v[48:49], off
	s_waitcnt vmcnt(7)
	v_mul_f32_e32 v48, v201, v191
	v_cmp_nge_f32_e32 vcc, s73, v48
	v_cmp_neq_f32_e64 s[38:39], 0, v207
	s_or_b64 vcc, vcc, s[38:39]
	s_cmp_lg_u64 vcc, 0
	s_cselect_b64 s[38:39], -1, 0
	s_cbranch_vccz .LBB0_1084
	v_sub_f32_e32 v95, v95, v207
	v_sub_f32_e32 v94, v94, v207
	v_sub_f32_e32 v93, v93, v207
	v_sub_f32_e32 v92, v92, v207
	v_sub_f32_e32 v91, v91, v207
	v_sub_f32_e32 v90, v90, v207
	v_sub_f32_e32 v89, v89, v207
	v_sub_f32_e32 v88, v88, v207
	v_sub_f32_e32 v87, v87, v207
	v_sub_f32_e32 v86, v86, v207
	v_sub_f32_e32 v85, v85, v207
	v_sub_f32_e32 v84, v84, v207
	v_sub_f32_e32 v83, v83, v207
	v_sub_f32_e32 v82, v82, v207
	v_sub_f32_e32 v81, v81, v207
	v_sub_f32_e32 v80, v80, v207
	v_sub_f32_e32 v111, v111, v207
	v_sub_f32_e32 v110, v110, v207
	v_sub_f32_e32 v109, v109, v207
	v_sub_f32_e32 v108, v108, v207
	v_sub_f32_e32 v107, v107, v207
	v_sub_f32_e32 v106, v106, v207
	v_sub_f32_e32 v105, v105, v207
	v_sub_f32_e32 v104, v104, v207
	v_sub_f32_e32 v103, v103, v207
	v_sub_f32_e32 v102, v102, v207
	v_sub_f32_e32 v101, v101, v207
	v_sub_f32_e32 v100, v100, v207
	v_sub_f32_e32 v99, v99, v207
	v_sub_f32_e32 v98, v98, v207
	v_sub_f32_e32 v97, v97, v207
	v_sub_f32_e32 v96, v96, v207
